# bias-partial sums: the 32 partial loads per element issued together (hipcc had a vmcnt(0) after each load), adds kept in the same order
# speedup vs baseline: 1.0037x; 1.0037x over previous
; __global__ void __launch_bounds__(NWAVES * 64, 2) mk_fwd(Args args) {
;     ...
;             for (int idx = vcu * (NWAVES * 64) + ftid; idx < nsb * F2; idx += G * (NWAVES * 64)) {
;                 const int sb = sb0 + idx / F2, n = idx % F2, s_ = sb % 3, kind_ = (sb / 3) % 3;
;                 const int nrows = s_ != 1 ? F2 : (kind_ == 0 ? 3 * D : (kind_ == 2 ? 2560 : 0));
;                 if (n < nrows) { float a = 0.f;
; #pragma unroll 8
;                     for (int kb = 0; kb < 32; ++kb) a += W_biasp[(size_t)kb * (DEPTH * 3 * F2) + (size_t)sb * F2 + n];
;                     W_bias[(size_t)sb * F2 + n] = a; }
;             }
.LBB0_1372:
	v_add_co_u32_e32 v10, vcc, 0x3c35c000, v4
	s_nop 1
	v_addc_co_u32_e32 v11, vcc, 0, v5, vcc
	global_load_dword v12, v[10:11], off
	v_add_co_u32_e32 v10, vcc, 0x3c3e0000, v4
	s_nop 1
	v_addc_co_u32_e32 v11, vcc, 0, v5, vcc
	global_load_dword v13, v[10:11], off
	v_add_co_u32_e32 v10, vcc, 0x3c464000, v4
	s_nop 1
	v_addc_co_u32_e32 v11, vcc, 0, v5, vcc
	global_load_dword v14, v[10:11], off
	v_add_co_u32_e32 v10, vcc, 0x3c4e8000, v4
	s_nop 1
	v_addc_co_u32_e32 v11, vcc, 0, v5, vcc
	global_load_dword v15, v[10:11], off
	v_add_co_u32_e32 v10, vcc, 0x3c56c000, v4
	s_nop 1
	v_addc_co_u32_e32 v11, vcc, 0, v5, vcc
	global_load_dword v16, v[10:11], off
	v_add_co_u32_e32 v10, vcc, 0x3c5f0000, v4
	s_nop 1
	v_addc_co_u32_e32 v11, vcc, 0, v5, vcc
	global_load_dword v17, v[10:11], off
	v_add_co_u32_e32 v10, vcc, 0x3c674000, v4
	s_nop 1
	v_addc_co_u32_e32 v11, vcc, 0, v5, vcc
	global_load_dword v18, v[10:11], off
	v_add_co_u32_e32 v10, vcc, 0x3c6f8000, v4
	s_nop 1
	v_addc_co_u32_e32 v11, vcc, 0, v5, vcc
	global_load_dword v19, v[10:11], off
	v_add_co_u32_e32 v10, vcc, 0x3c77c000, v4
	s_nop 1
	v_addc_co_u32_e32 v11, vcc, 0, v5, vcc
	global_load_dword v20, v[10:11], off
	v_add_co_u32_e32 v10, vcc, 0x3c800000, v4
	s_nop 1
	v_addc_co_u32_e32 v11, vcc, 0, v5, vcc
	global_load_dword v21, v[10:11], off
	v_add_co_u32_e32 v10, vcc, 0x3c884000, v4
	s_nop 1
	v_addc_co_u32_e32 v11, vcc, 0, v5, vcc
	global_load_dword v22, v[10:11], off
	v_add_co_u32_e32 v10, vcc, 0x3c908000, v4
	s_nop 1
	v_addc_co_u32_e32 v11, vcc, 0, v5, vcc
	global_load_dword v23, v[10:11], off
	v_add_co_u32_e32 v10, vcc, 0x3c98c000, v4
	s_nop 1
	v_addc_co_u32_e32 v11, vcc, 0, v5, vcc
	global_load_dword v24, v[10:11], off
	v_add_co_u32_e32 v10, vcc, 0x3ca10000, v4
	s_nop 1
	v_addc_co_u32_e32 v11, vcc, 0, v5, vcc
	global_load_dword v25, v[10:11], off
	v_add_co_u32_e32 v10, vcc, 0x3ca94000, v4
	s_nop 1
	v_addc_co_u32_e32 v11, vcc, 0, v5, vcc
	global_load_dword v26, v[10:11], off
	v_add_co_u32_e32 v10, vcc, 0x3cb18000, v4
	s_nop 1
	v_addc_co_u32_e32 v11, vcc, 0, v5, vcc
	global_load_dword v27, v[10:11], off
	v_add_co_u32_e32 v10, vcc, 0x3cb9c000, v4
	s_nop 1
	v_addc_co_u32_e32 v11, vcc, 0, v5, vcc
	global_load_dword v28, v[10:11], off
	v_add_co_u32_e32 v10, vcc, 0x3cc20000, v4
	s_nop 1
	v_addc_co_u32_e32 v11, vcc, 0, v5, vcc
	global_load_dword v29, v[10:11], off
	v_add_co_u32_e32 v10, vcc, 0x3cca4000, v4
	s_nop 1
	v_addc_co_u32_e32 v11, vcc, 0, v5, vcc
	global_load_dword v30, v[10:11], off
	v_add_co_u32_e32 v10, vcc, 0x3cd28000, v4
	s_nop 1
	v_addc_co_u32_e32 v11, vcc, 0, v5, vcc
	global_load_dword v31, v[10:11], off
	v_add_co_u32_e32 v10, vcc, 0x3cdac000, v4
	s_nop 1
	v_addc_co_u32_e32 v11, vcc, 0, v5, vcc
	global_load_dword v32, v[10:11], off
	v_add_co_u32_e32 v10, vcc, 0x3ce30000, v4
	s_nop 1
	v_addc_co_u32_e32 v11, vcc, 0, v5, vcc
	global_load_dword v33, v[10:11], off
	v_add_co_u32_e32 v10, vcc, 0x3ceb4000, v4
	s_nop 1
	v_addc_co_u32_e32 v11, vcc, 0, v5, vcc
	global_load_dword v34, v[10:11], off
	v_add_co_u32_e32 v10, vcc, 0x3cf38000, v4
	s_nop 1
	v_addc_co_u32_e32 v11, vcc, 0, v5, vcc
	global_load_dword v35, v[10:11], off
	v_add_co_u32_e32 v10, vcc, 0x3cfbc000, v4
	s_nop 1
	v_addc_co_u32_e32 v11, vcc, 0, v5, vcc
	global_load_dword v36, v[10:11], off
	v_add_co_u32_e32 v10, vcc, 0x3d040000, v4
	s_nop 1
	v_addc_co_u32_e32 v11, vcc, 0, v5, vcc
	global_load_dword v37, v[10:11], off
	v_add_co_u32_e32 v10, vcc, 0x3d0c4000, v4
	s_nop 1
	v_addc_co_u32_e32 v11, vcc, 0, v5, vcc
	global_load_dword v38, v[10:11], off
	v_add_co_u32_e32 v10, vcc, 0x3d148000, v4
	s_nop 1
	v_addc_co_u32_e32 v11, vcc, 0, v5, vcc
	global_load_dword v39, v[10:11], off
	v_add_co_u32_e32 v10, vcc, 0x3d1cc000, v4
	s_nop 1
	v_addc_co_u32_e32 v11, vcc, 0, v5, vcc
	global_load_dword v40, v[10:11], off
	v_add_co_u32_e32 v10, vcc, 0x3d250000, v4
	s_nop 1
	v_addc_co_u32_e32 v11, vcc, 0, v5, vcc
	global_load_dword v41, v[10:11], off
	v_add_co_u32_e32 v10, vcc, 0x3d2d4000, v4
	s_nop 1
	v_addc_co_u32_e32 v11, vcc, 0, v5, vcc
	global_load_dword v42, v[10:11], off
	v_add_co_u32_e32 v10, vcc, 0x3d358000, v4
	s_nop 1
	v_addc_co_u32_e32 v11, vcc, 0, v5, vcc
	global_load_dword v43, v[10:11], off
	s_waitcnt vmcnt(0)
	v_add_f32_e32 v7, v7, v12
	v_add_f32_e32 v7, v7, v13
	v_add_f32_e32 v7, v7, v14
	v_add_f32_e32 v7, v7, v15
	v_add_f32_e32 v7, v7, v16
	v_add_f32_e32 v7, v7, v17
	v_add_f32_e32 v7, v7, v18
	v_add_f32_e32 v7, v7, v19
	v_add_f32_e32 v7, v7, v20
	v_add_f32_e32 v7, v7, v21
	v_add_f32_e32 v7, v7, v22
	v_add_f32_e32 v7, v7, v23
	v_add_f32_e32 v7, v7, v24
	v_add_f32_e32 v7, v7, v25
	v_add_f32_e32 v7, v7, v26
	v_add_f32_e32 v7, v7, v27
	v_add_f32_e32 v7, v7, v28
	v_add_f32_e32 v7, v7, v29
	v_add_f32_e32 v7, v7, v30
	v_add_f32_e32 v7, v7, v31
	v_add_f32_e32 v7, v7, v32
	v_add_f32_e32 v7, v7, v33
	v_add_f32_e32 v7, v7, v34
	v_add_f32_e32 v7, v7, v35
	v_add_f32_e32 v7, v7, v36
	v_add_f32_e32 v7, v7, v37
	v_add_f32_e32 v7, v7, v38
	v_add_f32_e32 v7, v7, v39
	v_add_f32_e32 v7, v7, v40
	v_add_f32_e32 v7, v7, v41
	v_add_f32_e32 v7, v7, v42
	v_add_f32_e32 v7, v7, v43
	v_lshl_add_u64 v[2:3], s[48:49], 0, v[2:3]
	v_lshl_add_u64 v[0:1], v[0:1], 2, v[2:3]
	global_store_dword v[0:1], v7, off
	s_branch .LBB0_1369
